# adds: attention P.V blocks refill each V fragment right after the MFMA that consumed it (rolling LDS reads, counted lgkmcnt)
# speedup vs baseline: 1.0038x; 1.0038x over previous
.LBB0_700:
	v_lshl_add_u32 v0, s65, 14, v252
	v_exp_f32_e32 v148, v82
	v_exp_f32_e32 v149, v83
	v_exp_f32_e32 v150, v84
	v_exp_f32_e32 v151, v85
	v_exp_f32_e32 v152, v86
	v_exp_f32_e32 v153, v87
	v_exp_f32_e32 v154, v88
	v_exp_f32_e32 v155, v89
	v_exp_f32_e32 v156, v90
	v_exp_f32_e32 v157, v91
	v_exp_f32_e32 v158, v92
	v_exp_f32_e32 v159, v93
	v_exp_f32_e32 v144, v78
	v_exp_f32_e32 v145, v79
	v_exp_f32_e32 v146, v80
	v_exp_f32_e32 v147, v81
	ds_read_b64_tr_b16 v[78:79], v0 offset:49152
	ds_read_b64_tr_b16 v[80:81], v0 offset:49664
	ds_read_b64_tr_b16 v[82:83], v0 offset:53248
	ds_read_b64_tr_b16 v[84:85], v0 offset:53760
	ds_read_b64_tr_b16 v[86:87], v0 offset:57344
	ds_read_b64_tr_b16 v[88:89], v0 offset:57856
	ds_read_b64_tr_b16 v[90:91], v0 offset:61440
	ds_read_b64_tr_b16 v[92:93], v0 offset:61952
	v_exp_f32_e32 v132, v66
	v_exp_f32_e32 v133, v67
	v_exp_f32_e32 v134, v68
	v_exp_f32_e32 v135, v69
	v_exp_f32_e32 v136, v70
	v_exp_f32_e32 v137, v71
	v_exp_f32_e32 v138, v72
	v_exp_f32_e32 v139, v73
	v_exp_f32_e32 v140, v74
	v_exp_f32_e32 v141, v75
	v_exp_f32_e32 v142, v76
	v_exp_f32_e32 v143, v77
	v_exp_f32_e32 v160, v94
	v_exp_f32_e32 v161, v95
	v_exp_f32_e32 v162, v96
	v_exp_f32_e32 v163, v97
	v_cvt_pk_bf16_f32 v66, v148, v149
	v_cvt_pk_bf16_f32 v67, v150, v151
	v_cvt_pk_bf16_f32 v68, v152, v153
	v_cvt_pk_bf16_f32 v69, v154, v155
	v_cvt_pk_bf16_f32 v70, v156, v157
	v_cvt_pk_bf16_f32 v71, v158, v159
	v_cvt_pk_bf16_f32 v72, v160, v161
	v_cvt_pk_bf16_f32 v73, v162, v163
	v_cvt_pk_bf16_f32 v74, v132, v133
	v_cvt_pk_bf16_f32 v75, v134, v135
	v_cvt_pk_bf16_f32 v76, v136, v137
	v_cvt_pk_bf16_f32 v77, v138, v139
	v_cvt_pk_bf16_f32 v94, v140, v141
	v_cvt_pk_bf16_f32 v95, v142, v143
	v_cvt_pk_bf16_f32 v96, v144, v145
	v_cvt_pk_bf16_f32 v97, v146, v147
	s_waitcnt lgkmcnt(6)
	v_mfma_f32_32x32x16_bf16 v[50:65], v[66:69], v[78:81], v[50:65]
	ds_read_b64_tr_b16 v[78:79], v0 offset:50176
	ds_read_b64_tr_b16 v[80:81], v0 offset:50688
	s_waitcnt lgkmcnt(6)
	v_mfma_f32_32x32x16_bf16 v[34:49], v[66:69], v[82:85], v[34:49]
	ds_read_b64_tr_b16 v[82:83], v0 offset:54272
	ds_read_b64_tr_b16 v[84:85], v0 offset:54784
	s_waitcnt lgkmcnt(6)
	v_mfma_f32_32x32x16_bf16 v[18:33], v[66:69], v[86:89], v[18:33]
	ds_read_b64_tr_b16 v[86:87], v0 offset:58368
	ds_read_b64_tr_b16 v[88:89], v0 offset:58880
	s_waitcnt lgkmcnt(6)
	v_mfma_f32_32x32x16_bf16 v[2:17], v[66:69], v[90:93], v[2:17]
	ds_read_b64_tr_b16 v[90:91], v0 offset:62464
	ds_read_b64_tr_b16 v[92:93], v0 offset:62976
	s_waitcnt lgkmcnt(6)
	v_mfma_f32_32x32x16_bf16 v[50:65], v[70:73], v[78:81], v[50:65]
	ds_read_b64_tr_b16 v[78:79], v0 offset:51200
	ds_read_b64_tr_b16 v[80:81], v0 offset:51712
	s_waitcnt lgkmcnt(6)
	v_mfma_f32_32x32x16_bf16 v[34:49], v[70:73], v[82:85], v[34:49]
	ds_read_b64_tr_b16 v[82:83], v0 offset:55296
	ds_read_b64_tr_b16 v[84:85], v0 offset:55808
	s_waitcnt lgkmcnt(6)
	v_mfma_f32_32x32x16_bf16 v[18:33], v[70:73], v[86:89], v[18:33]
	ds_read_b64_tr_b16 v[86:87], v0 offset:59392
	ds_read_b64_tr_b16 v[88:89], v0 offset:59904
	s_waitcnt lgkmcnt(6)
	v_mfma_f32_32x32x16_bf16 v[2:17], v[70:73], v[90:93], v[2:17]
	ds_read_b64_tr_b16 v[90:91], v0 offset:63488
	ds_read_b64_tr_b16 v[92:93], v0 offset:64000
	s_waitcnt lgkmcnt(6)
	v_mfma_f32_32x32x16_bf16 v[50:65], v[74:77], v[78:81], v[50:65]
	ds_read_b64_tr_b16 v[78:79], v0 offset:52224
	ds_read_b64_tr_b16 v[80:81], v0 offset:52736
	s_waitcnt lgkmcnt(6)
	v_mfma_f32_32x32x16_bf16 v[34:49], v[74:77], v[82:85], v[34:49]
	ds_read_b64_tr_b16 v[82:83], v0 offset:56320
	ds_read_b64_tr_b16 v[84:85], v0 offset:56832
	s_waitcnt lgkmcnt(6)
	v_mfma_f32_32x32x16_bf16 v[18:33], v[74:77], v[86:89], v[18:33]
	ds_read_b64_tr_b16 v[86:87], v0 offset:60416
	ds_read_b64_tr_b16 v[88:89], v0 offset:60928
	s_waitcnt lgkmcnt(6)
	v_mfma_f32_32x32x16_bf16 v[2:17], v[74:77], v[90:93], v[2:17]
	ds_read_b64_tr_b16 v[90:91], v0 offset:64512
	ds_read_b64_tr_b16 v[92:93], v0 offset:65024
	s_waitcnt lgkmcnt(6)
	v_mfma_f32_32x32x16_bf16 v[50:65], v[94:97], v[78:81], v[50:65]
	s_waitcnt lgkmcnt(4)
	v_mfma_f32_32x32x16_bf16 v[34:49], v[94:97], v[82:85], v[34:49]
	s_waitcnt lgkmcnt(2)
	v_mfma_f32_32x32x16_bf16 v[18:33], v[94:97], v[86:89], v[18:33]
	s_waitcnt lgkmcnt(0)
	v_mfma_f32_32x32x16_bf16 v[2:17], v[94:97], v[90:93], v[2:17]
	s_mov_b64 s[34:35], -1
	s_and_b64 vcc, exec, s[28:29]
	s_cbranch_vccz .LBB0_708
	s_mov_b64 s[28:29], -1
	s_and_b64 vcc, exec, s[30:31]
	s_cbranch_vccz .LBB0_703
	s_waitcnt vmcnt(0) lgkmcnt(0)
	s_barrier
	s_mov_b64 s[28:29], 0

.LBB0_720:
	v_add_f32_e32 v133, v181, v182
	v_lshl_add_u32 v181, s47, 14, v252
	ds_read_b64_tr_b16 v[144:145], v181 offset:49152
	ds_read_b64_tr_b16 v[146:147], v181 offset:49664
	ds_read_b64_tr_b16 v[148:149], v181 offset:53248
	ds_read_b64_tr_b16 v[150:151], v181 offset:53760
	ds_read_b64_tr_b16 v[152:153], v181 offset:57344
	ds_read_b64_tr_b16 v[154:155], v181 offset:57856
	ds_read_b64_tr_b16 v[156:157], v181 offset:61440
	ds_read_b64_tr_b16 v[158:159], v181 offset:61952
	v_exp_f32_e32 v100, v100
	v_exp_f32_e32 v116, v116
	v_exp_f32_e32 v101, v101
	v_exp_f32_e32 v117, v117
	v_exp_f32_e32 v102, v102
	v_exp_f32_e32 v118, v118
	v_exp_f32_e32 v103, v103
	v_exp_f32_e32 v119, v119
	v_exp_f32_e32 v104, v104
	v_exp_f32_e32 v120, v120
	v_exp_f32_e32 v105, v105
	v_exp_f32_e32 v121, v121
	v_exp_f32_e32 v106, v106
	v_exp_f32_e32 v122, v122
	v_exp_f32_e32 v107, v107
	v_exp_f32_e32 v123, v123
	v_exp_f32_e32 v108, v108
	v_exp_f32_e32 v124, v124
	v_exp_f32_e32 v109, v109
	v_exp_f32_e32 v125, v125
	v_exp_f32_e32 v110, v110
	v_exp_f32_e32 v126, v126
	v_exp_f32_e32 v111, v111
	v_exp_f32_e32 v127, v127
	v_exp_f32_e32 v112, v112
	v_exp_f32_e32 v128, v128
	v_exp_f32_e32 v113, v113
	v_exp_f32_e32 v129, v129
	v_exp_f32_e32 v114, v114
	v_exp_f32_e32 v130, v130
	v_exp_f32_e32 v115, v115
	v_exp_f32_e32 v131, v131
	v_add_f32_e32 v132, v183, v132
	v_max3_f32 v180, v180, v133, v132
	v_cvt_pk_bf16_f32 v132, v100, v101
	v_cvt_pk_bf16_f32 v133, v102, v103
	v_cvt_pk_bf16_f32 v134, v104, v105
	v_cvt_pk_bf16_f32 v135, v106, v107
	v_cvt_pk_bf16_f32 v136, v108, v109
	v_cvt_pk_bf16_f32 v137, v110, v111
	v_cvt_pk_bf16_f32 v138, v112, v113
	v_cvt_pk_bf16_f32 v139, v114, v115
	v_cvt_pk_bf16_f32 v140, v116, v117
	v_cvt_pk_bf16_f32 v141, v118, v119
	v_cvt_pk_bf16_f32 v142, v120, v121
	v_cvt_pk_bf16_f32 v143, v122, v123
	v_cvt_pk_bf16_f32 v160, v124, v125
	v_cvt_pk_bf16_f32 v161, v126, v127
	v_cvt_pk_bf16_f32 v162, v128, v129
	v_cvt_pk_bf16_f32 v163, v130, v131
	s_waitcnt lgkmcnt(6)
	v_mfma_f32_32x32x16_bf16 v[50:65], v[132:135], v[144:147], v[50:65]
	ds_read_b64_tr_b16 v[144:145], v181 offset:50176
	ds_read_b64_tr_b16 v[146:147], v181 offset:50688
	s_waitcnt lgkmcnt(6)
	v_mfma_f32_32x32x16_bf16 v[34:49], v[132:135], v[148:151], v[34:49]
	ds_read_b64_tr_b16 v[148:149], v181 offset:54272
	ds_read_b64_tr_b16 v[150:151], v181 offset:54784
	s_waitcnt lgkmcnt(6)
	v_mfma_f32_32x32x16_bf16 v[18:33], v[132:135], v[152:155], v[18:33]
	ds_read_b64_tr_b16 v[152:153], v181 offset:58368
	ds_read_b64_tr_b16 v[154:155], v181 offset:58880
	s_waitcnt lgkmcnt(6)
	v_mfma_f32_32x32x16_bf16 v[2:17], v[132:135], v[156:159], v[2:17]
	ds_read_b64_tr_b16 v[156:157], v181 offset:62464
	ds_read_b64_tr_b16 v[158:159], v181 offset:62976
	s_waitcnt lgkmcnt(6)
	v_mfma_f32_32x32x16_bf16 v[50:65], v[136:139], v[144:147], v[50:65]
	ds_read_b64_tr_b16 v[144:145], v181 offset:51200
	ds_read_b64_tr_b16 v[146:147], v181 offset:51712
	s_waitcnt lgkmcnt(6)
	v_mfma_f32_32x32x16_bf16 v[34:49], v[136:139], v[148:151], v[34:49]
	ds_read_b64_tr_b16 v[148:149], v181 offset:55296
	ds_read_b64_tr_b16 v[150:151], v181 offset:55808
	s_waitcnt lgkmcnt(6)
	v_mfma_f32_32x32x16_bf16 v[18:33], v[136:139], v[152:155], v[18:33]
	ds_read_b64_tr_b16 v[152:153], v181 offset:59392
	ds_read_b64_tr_b16 v[154:155], v181 offset:59904
	s_waitcnt lgkmcnt(6)
	v_mfma_f32_32x32x16_bf16 v[2:17], v[136:139], v[156:159], v[2:17]
	ds_read_b64_tr_b16 v[156:157], v181 offset:63488
	ds_read_b64_tr_b16 v[158:159], v181 offset:64000
	s_waitcnt lgkmcnt(6)
	v_mfma_f32_32x32x16_bf16 v[50:65], v[140:143], v[144:147], v[50:65]
	ds_read_b64_tr_b16 v[144:145], v181 offset:52224
	ds_read_b64_tr_b16 v[146:147], v181 offset:52736
	s_waitcnt lgkmcnt(6)
	v_mfma_f32_32x32x16_bf16 v[34:49], v[140:143], v[148:151], v[34:49]
	ds_read_b64_tr_b16 v[148:149], v181 offset:56320
	ds_read_b64_tr_b16 v[150:151], v181 offset:56832
	s_waitcnt lgkmcnt(6)
	v_mfma_f32_32x32x16_bf16 v[18:33], v[140:143], v[152:155], v[18:33]
	ds_read_b64_tr_b16 v[152:153], v181 offset:60416
	ds_read_b64_tr_b16 v[154:155], v181 offset:60928
	s_waitcnt lgkmcnt(6)
	v_mfma_f32_32x32x16_bf16 v[2:17], v[140:143], v[156:159], v[2:17]
	ds_read_b64_tr_b16 v[156:157], v181 offset:64512
	ds_read_b64_tr_b16 v[158:159], v181 offset:65024
	s_waitcnt lgkmcnt(6)
	v_mfma_f32_32x32x16_bf16 v[50:65], v[160:163], v[144:147], v[50:65]
	s_waitcnt lgkmcnt(4)
	v_mfma_f32_32x32x16_bf16 v[34:49], v[160:163], v[148:151], v[34:49]
	s_waitcnt lgkmcnt(2)
	v_mfma_f32_32x32x16_bf16 v[18:33], v[160:163], v[152:155], v[18:33]
	s_waitcnt lgkmcnt(0)
	v_mfma_f32_32x32x16_bf16 v[2:17], v[160:163], v[156:159], v[2:17]
	s_cmp_lg_u32 s44, 4
	s_cbranch_scc1 .LBB0_724
	v_xor_b32_e32 v132, 0x80000000, v180
	v_max_f32_e64 v133, -v180, -v180
	s_nop 0
	v_mov_b32_dpp v132, v132 quad_perm:[1,0,3,2] row_mask:0xf bank_mask:0xf bound_ctrl:1
	v_max_f32_e32 v132, v132, v132
	v_max_f32_e32 v132, v133, v132
	s_nop 1
	v_mov_b32_dpp v133, v132 quad_perm:[2,3,0,1] row_mask:0xf bank_mask:0xf bound_ctrl:1
	v_max_f32_e32 v133, v133, v133
	v_max_f32_e32 v132, v132, v133
	s_nop 1
	v_mov_b32_dpp v133, v132 row_half_mirror row_mask:0xf bank_mask:0xf bound_ctrl:1
	v_max_f32_e32 v133, v133, v133
	v_max_f32_e32 v132, v132, v133
	s_nop 1
	v_mov_b32_dpp v133, v132 row_mirror row_mask:0xf bank_mask:0xf bound_ctrl:1
	v_max_f32_e32 v133, v133, v133
	v_max_f32_e32 v132, v132, v133
	v_mov_b32_e32 v133, v132
	s_nop 1
	v_permlane16_swap_b32 v132, v133
	s_nop 0
	v_max_f32_e32 v132, v132, v132
	v_max_f32_e32 v133, v133, v133
	v_max_f32_e32 v132, v133, v132
	v_mov_b32_e32 v133, v132
	s_nop 1
	v_permlane32_swap_b32 v132, v133
	s_and_saveexec_b64 s[24:25], s[6:7]
	s_cbranch_execz .LBB0_723
	v_max_f32_e64 v132, -v132, -v132
	v_max_f32_e64 v133, -v133, -v133
	v_min_f32_e32 v132, v133, v132
	v_sub_f32_e32 v132, v132, v251
	v_add_f32_e32 v132, 0xc2180000, v132
	v_div_scale_f32 v133, s[26:27], v188, v188, v132
	v_rcp_f32_e32 v134, v133
	s_nop 0
	v_fma_f32 v135, -v133, v134, 1.0
	v_fmac_f32_e32 v134, v135, v134
	v_div_scale_f32 v135, vcc, v132, v188, v132
	v_mul_f32_e32 v136, v135, v134
	v_fma_f32 v137, -v133, v136, v135
	v_fmac_f32_e32 v136, v137, v134
	v_fma_f32 v133, -v133, v136, v135
	v_div_fmas_f32 v133, v133, v134, v136
	v_div_fixup_f32 v132, v133, v188, v132
	v_add_f32_e32 v132, v132, v99
	v_add_f32_e32 v132, 0xc27c0000, v132
	v_mov_b32_e32 v133, s42
	ds_write_b32 v133, v132 offset:32
